# baseline (speedup 1.0000x reference)
_Z13attend_kernelPKfS0_S0_S0_S0_S0_S0_S0_S0_S0_PDF16_:
	s_and_b32 s22, s2, 7
	s_lshr_b32 s24, s2, 1
	s_and_b32 s23, s24, 0x7ffffffc
	s_lshl_b32 s24, s22, 7
	s_add_i32 s24, s24, s23
	s_load_dwordx2 s[14:15], s[0:1], 0x8
	s_load_dwordx4 s[4:7], s[0:1], 0x10
	s_load_dwordx2 s[16:17], s[0:1], 0x20
	s_load_dwordx4 s[8:11], s[0:1], 0x28
	s_load_dwordx4 s[28:31], s[0:1], 0x38
	s_load_dwordx2 s[18:19], s[0:1], 0x48
	s_load_dwordx2 s[12:13], s[0:1], 0x50
	s_load_dwordx2 s[2:3], s[0:1], 0x0
	v_mov_b32_e32 v70, s24
	s_movk_i32 s25, 0x12c
	v_mul_u32_u24_e32 v1, 0x1b5, v0
	v_lshrrev_b32_e32 v1, 16, v1
	v_mul_u32_u24_e32 v2, 0x96, v1
	v_sub_u32_e32 v2, v0, v2
	v_add_u32_e32 v3, s24, v1
	v_mad_u32_u24 v3, v3, s25, v2
	v_lshlrev_b32_e32 v3, 2, v3
	v_mul_u32_u24_e32 v7, 0x260, v1
	v_lshl_add_u32 v7, v2, 2, v7
	v_mov_b32_e32 v5, 0
	v_mov_b32_e32 v6, 0
	v_lshrrev_b32_e32 v8, 2, v0
	v_mul_u32_u24_e32 v8, 0x6d3b, v8
	v_lshrrev_b32_e32 v8, 21, v8
	v_mul_u32_u24_e32 v9, 0x12c, v8
	v_sub_u32_e32 v9, v0, v9
	v_add_u32_e32 v10, s24, v8
	v_mad_u32_u24 v10, v10, s25, v9
	v_lshlrev_b32_e32 v10, 2, v10
	v_mul_u32_u24_e32 v12, 0x4c0, v8
	v_lshl_add_u32 v12, v9, 2, v12
	s_add_i32 s27, s24, 3
	s_mul_i32 s27, s27, 0x12c
	s_add_i32 s27, s27, 0x7c
	s_lshl_b32 s27, s27, 2
	v_lshl_add_u32 v9, v0, 2, s27
	v_lshlrev_b32_e32 v4, 2, v0
	v_add_u32_e32 v8, 0xfffffd80, v0
	v_lshlrev_b32_e32 v14, 2, v8
	v_mov_b32_e32 v15, 0
	v_mov_b32_e32 v16, 0
	v_lshrrev_b32_e32 v17, 7, v0
	v_and_b32_e32 v18, 0x7f, v0
	v_add_u32_e32 v19, s24, v17
	v_lshl_or_b32 v19, v19, 7, v18
	v_lshlrev_b32_e32 v19, 2, v19
	v_add_u32_e32 v20, 0x100000, v19
	v_lshlrev_b32_e32 v21, 9, v17
	v_lshl_or_b32 v21, v18, 2, v21
	s_waitcnt lgkmcnt(0)
	s_movk_i32 s26, 0x258
	v_cmp_gt_u32_e32 vcc, s26, v0
	s_and_saveexec_b64 s[20:21], vcc
	global_load_dword v5, v3, s[8:9]
	global_load_dword v6, v3, s[10:11]
	s_or_b64 exec, exec, s[20:21]
	global_load_dword v11, v10, s[14:15]
	s_movk_i32 s26, 0xb0
	v_cmp_gt_u32_e32 vcc, s26, v0
	s_and_saveexec_b64 s[20:21], vcc
	global_load_dword v13, v9, s[14:15]
	s_or_b64 exec, exec, s[20:21]
	s_movk_i32 s26, 0x96
	v_cmp_gt_u32_e32 vcc, s26, v8
	s_and_saveexec_b64 s[20:21], vcc
	global_load_dword v15, v14, s[28:29]
	global_load_dword v16, v14, s[30:31]
	s_or_b64 exec, exec, s[20:21]
	s_movk_i32 s26, 0x200
	v_cmp_gt_u32_e32 vcc, s26, v0
	s_and_saveexec_b64 s[20:21], vcc
	global_load_dword v22, v19, s[18:19]
	global_load_dword v23, v20, s[18:19]
	s_or_b64 exec, exec, s[20:21]
	v_lshrrev_b32_e32 v118, 7, v0
	v_and_b32_e32 v119, 0x7f, v0
	s_mul_i32 s26, s22, 0x2ee
	s_mov_b64 s[20:21], 0x1000
	v_mul_u32_u24_e32 v120, 38, v118
	v_add_lshl_u32 v120, s26, v120, 9
	v_mov_b32_e32 v121, 0
	v_lshl_add_u64 v[122:123], s[16:17], 0, v[120:121]
	v_lshlrev_b32_e32 v120, 2, v119
	v_lshl_add_u64 v[122:123], v[122:123], 0, v[120:121]
	global_load_dword v80, v[122:123], off
	global_load_dword v81, v[122:123], off offset:512
	global_load_dword v82, v[122:123], off offset:1024
	global_load_dword v83, v[122:123], off offset:1536
	global_load_dword v84, v[122:123], off offset:2048
	global_load_dword v85, v[122:123], off offset:2560
	global_load_dword v86, v[122:123], off offset:3072
	global_load_dword v87, v[122:123], off offset:3584
	v_lshl_add_u64 v[122:123], v[122:123], 0, s[20:21]
	global_load_dword v88, v[122:123], off
	global_load_dword v89, v[122:123], off offset:512
	global_load_dword v90, v[122:123], off offset:1024
	global_load_dword v91, v[122:123], off offset:1536
	global_load_dword v92, v[122:123], off offset:2048
	global_load_dword v93, v[122:123], off offset:2560
	global_load_dword v94, v[122:123], off offset:3072
	global_load_dword v95, v[122:123], off offset:3584
	v_lshl_add_u64 v[122:123], v[122:123], 0, s[20:21]
	global_load_dword v96, v[122:123], off
	global_load_dword v97, v[122:123], off offset:512
	global_load_dword v98, v[122:123], off offset:1024
	global_load_dword v99, v[122:123], off offset:1536
	global_load_dword v100, v[122:123], off offset:2048
	global_load_dword v101, v[122:123], off offset:2560
	global_load_dword v102, v[122:123], off offset:3072
	global_load_dword v103, v[122:123], off offset:3584
	v_lshl_add_u64 v[122:123], v[122:123], 0, s[20:21]
	global_load_dword v104, v[122:123], off
	global_load_dword v105, v[122:123], off offset:512
	global_load_dword v106, v[122:123], off offset:1024
	global_load_dword v107, v[122:123], off offset:1536
	global_load_dword v108, v[122:123], off offset:2048
	global_load_dword v109, v[122:123], off offset:2560
	global_load_dword v110, v[122:123], off offset:3072
	global_load_dword v111, v[122:123], off offset:3584
	v_lshl_add_u64 v[122:123], v[122:123], 0, s[20:21]
	global_load_dword v112, v[122:123], off
	global_load_dword v113, v[122:123], off offset:512
	global_load_dword v114, v[122:123], off offset:1024
	global_load_dword v115, v[122:123], off offset:1536
	global_load_dword v116, v[122:123], off offset:2048
	global_load_dword v117, v[122:123], off offset:2560
	s_waitcnt vmcnt(38)
	s_mov_b32 s26, 0xc27c0000
	v_mov_b32_e32 v24, 0x427c0000
	v_mul_f32_e32 v5, 0x4038aa3b, v5
	v_mul_f32_e32 v6, 0xc038aa3b, v6
	v_med3_f32 v5, v5, s26, v24
	v_med3_f32 v6, v6, s26, v24
	v_exp_f32_e32 v5, v5
	v_exp_f32_e32 v6, v6
	s_movk_i32 s26, 0x258
	v_cmp_gt_u32_e32 vcc, s26, v0
	s_and_saveexec_b64 s[20:21], vcc
	ds_write_b32 v7, v5 offset:64256
	v_add_u32_e32 v25, 0x10480, v7
	ds_write_b32 v25, v6
	s_or_b64 exec, exec, s[20:21]
	ds_write_b32 v12, v11 offset:59392
	s_movk_i32 s26, 0xb0
	v_cmp_gt_u32_e32 vcc, s26, v0
	s_and_saveexec_b64 s[20:21], vcc
	ds_write_b32 v4, v13 offset:63536
	s_or_b64 exec, exec, s[20:21]
	s_movk_i32 s26, 0x98
	v_cmp_gt_u32_e32 vcc, s26, v8
	s_and_saveexec_b64 s[20:21], vcc
	v_add_u32_e32 v25, 0x10e00, v14
	ds_write_b32 v25, v15
	v_add_u32_e32 v25, 0x11060, v14
	ds_write_b32 v25, v16
	s_or_b64 exec, exec, s[20:21]
	v_mov_b32_e32 v26, 0
	v_add_u32_e32 v25, 0xfffffce0, v0
	v_cmp_gt_u32_e32 vcc, 16, v25
	s_and_saveexec_b64 s[20:21], vcc
	v_lshrrev_b32_e32 v27, 2, v25
	v_mul_u32_u24_e32 v27, 0x4c0, v27
	v_and_b32_e32 v25, 3, v25
	v_lshl_add_u32 v27, v25, 2, v27
	ds_write_b32 v27, v26 offset:60592
	s_or_b64 exec, exec, s[20:21]
	v_add_u32_e32 v25, 0xfffffcc0, v0
	v_cmp_gt_u32_e32 vcc, 8, v25
	s_and_saveexec_b64 s[20:21], vcc
	v_lshrrev_b32_e32 v27, 1, v25
	v_mul_u32_u24_e32 v27, 0x260, v27
	v_and_b32_e32 v25, 1, v25
	v_lshl_add_u32 v27, v25, 2, v27
	ds_write_b32 v27, v26 offset:64856
	v_add_u32_e32 v27, 0x106d8, v27
	ds_write_b32 v27, v26
	s_or_b64 exec, exec, s[20:21]
	s_movk_i32 s26, 0x200
	v_cmp_gt_u32_e32 vcc, s26, v0
	s_and_saveexec_b64 s[20:21], vcc
	v_add_u32_e32 v21, 0xc000, v21
	ds_write_b32 v21, v22
	ds_write_b32 v21, v23 offset:4096
	s_or_b64 exec, exec, s[20:21]
	v_lshrrev_b32_e32 v1, 7, v0
	v_and_b32_e32 v2, 0x7f, v0
	v_lshlrev_b32_e32 v38, 2, v2
	s_mul_i32 s8, s22, 0x2ee
	s_mov_b64 s[0:1], 0x1000
	v_mov_b32_e32 v5, 0
	v_mov_b32_e32 v6, v38
	v_mov_b32_e32 v7, 0
	v_mul_u32_u24_e32 v3, 19, v1
	v_add_lshl_u32 v4, s8, v3, 9
	v_lshl_add_u64 v[42:43], s[4:5], 0, v[4:5]
	v_lshl_add_u64 v[42:43], v[42:43], 0, v[6:7]
	v_lshl_add_u64 v[44:45], s[6:7], 0, v[4:5]
	v_lshl_add_u64 v[44:45], v[44:45], 0, v[6:7]
	v_mul_u32_u24_e32 v39, 0x98, v1
	v_add_u32_e32 v39, 0xe800, v39
	v_add_u32_e32 v71, 0x980, v39
	global_load_dword v2, v[42:43], off
	global_load_dword v3, v[44:45], off
	global_load_dword v4, v[42:43], off offset:512
	global_load_dword v5, v[44:45], off offset:512
	global_load_dword v6, v[42:43], off offset:1024
	global_load_dword v7, v[44:45], off offset:1024
	global_load_dword v8, v[42:43], off offset:1536
	global_load_dword v9, v[44:45], off offset:1536
	global_load_dword v10, v[42:43], off offset:2048
	global_load_dword v11, v[44:45], off offset:2048
	global_load_dword v12, v[42:43], off offset:2560
	global_load_dword v13, v[44:45], off offset:2560
	global_load_dword v14, v[42:43], off offset:3072
	global_load_dword v15, v[44:45], off offset:3072
	global_load_dword v16, v[42:43], off offset:3584
	global_load_dword v17, v[44:45], off offset:3584
	v_lshl_add_u64 v[42:43], v[42:43], 0, s[0:1]
	v_lshl_add_u64 v[44:45], v[44:45], 0, s[0:1]
	global_load_dword v18, v[42:43], off
	global_load_dword v19, v[44:45], off
	global_load_dword v20, v[42:43], off offset:512
	global_load_dword v21, v[44:45], off offset:512
	global_load_dword v22, v[42:43], off offset:1024
	global_load_dword v23, v[44:45], off offset:1024
	global_load_dword v24, v[42:43], off offset:1536
	global_load_dword v25, v[44:45], off offset:1536
	global_load_dword v26, v[42:43], off offset:2048
	global_load_dword v27, v[44:45], off offset:2048
	global_load_dword v28, v[42:43], off offset:2560
	global_load_dword v29, v[44:45], off offset:2560
	global_load_dword v30, v[42:43], off offset:3072
	global_load_dword v31, v[44:45], off offset:3072
	global_load_dword v32, v[42:43], off offset:3584
	global_load_dword v33, v[44:45], off offset:3584
	v_lshl_add_u64 v[42:43], v[42:43], 0, s[0:1]
	v_lshl_add_u64 v[44:45], v[44:45], 0, s[0:1]
	global_load_dword v34, v[42:43], off
	global_load_dword v35, v[44:45], off
	global_load_dword v36, v[42:43], off offset:512
	global_load_dword v37, v[44:45], off offset:512
	global_load_dword v118, v[42:43], off offset:1024
	global_load_dword v119, v[44:45], off offset:1024
	v_mov_b32_e32 v76, 0
	v_mov_b32_e32 v77, 0
	v_mov_b32_e32 v78, 0
	v_mov_b32_e32 v79, 0
	v_mov_b32_e32 v120, 0
	v_mov_b32_e32 v121, 0
	v_mov_b32_e32 v122, 0
	v_mov_b32_e32 v123, 0
	s_waitcnt lgkmcnt(0)
	s_barrier
	ds_read2_b64 v[40:43], v39 offset0:0 offset1:1
	ds_read2_b64 v[44:47], v39 offset0:152 offset1:153
	ds_read2_b64 v[48:51], v71 offset0:0 offset1:1
	ds_read2_b64 v[52:55], v71 offset0:152 offset1:153
	ds_read2_b64 v[56:59], v39 offset0:2 offset1:3
	ds_read2_b64 v[60:63], v39 offset0:154 offset1:155
	ds_read2_b64 v[64:67], v71 offset0:2 offset1:3
	ds_read2_b64 v[72:75], v71 offset0:154 offset1:155
	s_waitcnt vmcnt(38) lgkmcnt(4)
	v_pk_fma_f32 v[76:77], v[40:41], v[80:81], v[76:77]
	v_pk_fma_f32 v[78:79], v[44:45], v[80:81], v[78:79]
	v_pk_fma_f32 v[120:121], v[48:49], v[80:81], v[120:121]
	v_pk_fma_f32 v[122:123], v[52:53], v[80:81], v[122:123]
	v_pk_fma_f32 v[76:77], v[42:43], v[82:83], v[76:77]
	v_pk_fma_f32 v[78:79], v[46:47], v[82:83], v[78:79]
	v_pk_fma_f32 v[120:121], v[50:51], v[82:83], v[120:121]
	v_pk_fma_f32 v[122:123], v[54:55], v[82:83], v[122:123]
	ds_read2_b64 v[40:43], v39 offset0:4 offset1:5
	ds_read2_b64 v[44:47], v39 offset0:156 offset1:157
	ds_read2_b64 v[48:51], v71 offset0:4 offset1:5
	ds_read2_b64 v[52:55], v71 offset0:156 offset1:157
	s_waitcnt vmcnt(38) lgkmcnt(4)
	v_pk_fma_f32 v[76:77], v[56:57], v[84:85], v[76:77]
	v_pk_fma_f32 v[78:79], v[60:61], v[84:85], v[78:79]
	v_pk_fma_f32 v[120:121], v[64:65], v[84:85], v[120:121]
	v_pk_fma_f32 v[122:123], v[72:73], v[84:85], v[122:123]
	v_pk_fma_f32 v[76:77], v[58:59], v[86:87], v[76:77]
	v_pk_fma_f32 v[78:79], v[62:63], v[86:87], v[78:79]
	v_pk_fma_f32 v[120:121], v[66:67], v[86:87], v[120:121]
	v_pk_fma_f32 v[122:123], v[74:75], v[86:87], v[122:123]
	ds_read2_b64 v[56:59], v39 offset0:6 offset1:7
	ds_read2_b64 v[60:63], v39 offset0:158 offset1:159
	ds_read2_b64 v[64:67], v71 offset0:6 offset1:7
	ds_read2_b64 v[72:75], v71 offset0:158 offset1:159
	s_waitcnt vmcnt(38) lgkmcnt(4)
	v_pk_fma_f32 v[76:77], v[40:41], v[88:89], v[76:77]
	v_pk_fma_f32 v[78:79], v[44:45], v[88:89], v[78:79]
	v_pk_fma_f32 v[120:121], v[48:49], v[88:89], v[120:121]
	v_pk_fma_f32 v[122:123], v[52:53], v[88:89], v[122:123]
	v_pk_fma_f32 v[76:77], v[42:43], v[90:91], v[76:77]
	v_pk_fma_f32 v[78:79], v[46:47], v[90:91], v[78:79]
	v_pk_fma_f32 v[120:121], v[50:51], v[90:91], v[120:121]
	v_pk_fma_f32 v[122:123], v[54:55], v[90:91], v[122:123]
	ds_read2_b64 v[40:43], v39 offset0:8 offset1:9
	ds_read2_b64 v[44:47], v39 offset0:160 offset1:161
	ds_read2_b64 v[48:51], v71 offset0:8 offset1:9
	ds_read2_b64 v[52:55], v71 offset0:160 offset1:161
	s_waitcnt vmcnt(38) lgkmcnt(4)
	v_pk_fma_f32 v[76:77], v[56:57], v[92:93], v[76:77]
	v_pk_fma_f32 v[78:79], v[60:61], v[92:93], v[78:79]
	v_pk_fma_f32 v[120:121], v[64:65], v[92:93], v[120:121]
	v_pk_fma_f32 v[122:123], v[72:73], v[92:93], v[122:123]
	v_pk_fma_f32 v[76:77], v[58:59], v[94:95], v[76:77]
	v_pk_fma_f32 v[78:79], v[62:63], v[94:95], v[78:79]
	v_pk_fma_f32 v[120:121], v[66:67], v[94:95], v[120:121]
	v_pk_fma_f32 v[122:123], v[74:75], v[94:95], v[122:123]
	ds_read2_b64 v[56:59], v39 offset0:10 offset1:11
	ds_read2_b64 v[60:63], v39 offset0:162 offset1:163
	ds_read2_b64 v[64:67], v71 offset0:10 offset1:11
	ds_read2_b64 v[72:75], v71 offset0:162 offset1:163
	s_waitcnt vmcnt(38) lgkmcnt(4)
	v_pk_fma_f32 v[76:77], v[40:41], v[96:97], v[76:77]
	v_pk_fma_f32 v[78:79], v[44:45], v[96:97], v[78:79]
	v_pk_fma_f32 v[120:121], v[48:49], v[96:97], v[120:121]
	v_pk_fma_f32 v[122:123], v[52:53], v[96:97], v[122:123]
	v_pk_fma_f32 v[76:77], v[42:43], v[98:99], v[76:77]
	v_pk_fma_f32 v[78:79], v[46:47], v[98:99], v[78:79]
	v_pk_fma_f32 v[120:121], v[50:51], v[98:99], v[120:121]
	v_pk_fma_f32 v[122:123], v[54:55], v[98:99], v[122:123]
	ds_read2_b64 v[40:43], v39 offset0:12 offset1:13
	ds_read2_b64 v[44:47], v39 offset0:164 offset1:165
	ds_read2_b64 v[48:51], v71 offset0:12 offset1:13
	ds_read2_b64 v[52:55], v71 offset0:164 offset1:165
	s_waitcnt vmcnt(38) lgkmcnt(4)
	v_pk_fma_f32 v[76:77], v[56:57], v[100:101], v[76:77]
	v_pk_fma_f32 v[78:79], v[60:61], v[100:101], v[78:79]
	v_pk_fma_f32 v[120:121], v[64:65], v[100:101], v[120:121]
	v_pk_fma_f32 v[122:123], v[72:73], v[100:101], v[122:123]
	v_pk_fma_f32 v[76:77], v[58:59], v[102:103], v[76:77]
	v_pk_fma_f32 v[78:79], v[62:63], v[102:103], v[78:79]
	v_pk_fma_f32 v[120:121], v[66:67], v[102:103], v[120:121]
	v_pk_fma_f32 v[122:123], v[74:75], v[102:103], v[122:123]
	ds_read2_b64 v[56:59], v39 offset0:14 offset1:15
	ds_read2_b64 v[60:63], v39 offset0:166 offset1:167
	ds_read2_b64 v[64:67], v71 offset0:14 offset1:15
	ds_read2_b64 v[72:75], v71 offset0:166 offset1:167
	s_waitcnt vmcnt(38) lgkmcnt(4)
	v_pk_fma_f32 v[76:77], v[40:41], v[104:105], v[76:77]
	v_pk_fma_f32 v[78:79], v[44:45], v[104:105], v[78:79]
	v_pk_fma_f32 v[120:121], v[48:49], v[104:105], v[120:121]
	v_pk_fma_f32 v[122:123], v[52:53], v[104:105], v[122:123]
	v_pk_fma_f32 v[76:77], v[42:43], v[106:107], v[76:77]
	v_pk_fma_f32 v[78:79], v[46:47], v[106:107], v[78:79]
	v_pk_fma_f32 v[120:121], v[50:51], v[106:107], v[120:121]
	v_pk_fma_f32 v[122:123], v[54:55], v[106:107], v[122:123]
	ds_read2_b64 v[40:43], v39 offset0:16 offset1:17
	ds_read2_b64 v[44:47], v39 offset0:168 offset1:169
	ds_read2_b64 v[48:51], v71 offset0:16 offset1:17
	ds_read2_b64 v[52:55], v71 offset0:168 offset1:169
	s_waitcnt vmcnt(38) lgkmcnt(4)
	v_pk_fma_f32 v[76:77], v[56:57], v[108:109], v[76:77]
	v_pk_fma_f32 v[78:79], v[60:61], v[108:109], v[78:79]
	v_pk_fma_f32 v[120:121], v[64:65], v[108:109], v[120:121]
	v_pk_fma_f32 v[122:123], v[72:73], v[108:109], v[122:123]
	v_pk_fma_f32 v[76:77], v[58:59], v[110:111], v[76:77]
	v_pk_fma_f32 v[78:79], v[62:63], v[110:111], v[78:79]
	v_pk_fma_f32 v[120:121], v[66:67], v[110:111], v[120:121]
	v_pk_fma_f32 v[122:123], v[74:75], v[110:111], v[122:123]
	ds_read2_b64 v[56:59], v39 offset0:18 offset1:19
	ds_read2_b64 v[60:63], v39 offset0:170 offset1:171
	ds_read2_b64 v[64:67], v71 offset0:18 offset1:19
	ds_read2_b64 v[72:75], v71 offset0:170 offset1:171
	s_waitcnt vmcnt(38) lgkmcnt(4)
	v_pk_fma_f32 v[76:77], v[40:41], v[112:113], v[76:77]
	v_pk_fma_f32 v[78:79], v[44:45], v[112:113], v[78:79]
	v_pk_fma_f32 v[120:121], v[48:49], v[112:113], v[120:121]
	v_pk_fma_f32 v[122:123], v[52:53], v[112:113], v[122:123]
	v_pk_fma_f32 v[76:77], v[42:43], v[114:115], v[76:77]
	v_pk_fma_f32 v[78:79], v[46:47], v[114:115], v[78:79]
	v_pk_fma_f32 v[120:121], v[50:51], v[114:115], v[120:121]
	v_pk_fma_f32 v[122:123], v[54:55], v[114:115], v[122:123]
	s_waitcnt vmcnt(38) lgkmcnt(0)
	v_pk_fma_f32 v[76:77], v[56:57], v[116:117], v[76:77]
	v_pk_fma_f32 v[78:79], v[60:61], v[116:117], v[78:79]
	v_pk_fma_f32 v[120:121], v[64:65], v[116:117], v[120:121]
	v_pk_fma_f32 v[122:123], v[72:73], v[116:117], v[122:123]
	v_mul_u32_u24_e32 v92, 0x4c, v1
	v_add_u32_e32 v92, 0xfb00, v92
	v_add_u32_e32 v93, 0x4c0, v92
	v_add_u32_e32 v94, 0x980, v92
	v_add_u32_e32 v95, 0xe40, v92
	v_add_u32_e32 v96, 0x1300, v92
	v_mov_b32_e32 v97, 0x427c0000
	s_mov_b32 s0, 0xc27c0000
	v_mov_b32_e32 v124, 1.0
	v_mov_b32_e32 v125, 1.0
	v_mov_b32_e32 v126, 0x4038aa3b
	v_mov_b32_e32 v127, 0x4038aa3b
	v_mov_b32_e32 v80, 0
	v_mov_b32_e32 v81, 0
	v_mov_b32_e32 v82, 0
	v_mov_b32_e32 v83, 0
	v_mov_b32_e32 v84, 0
	v_mov_b32_e32 v85, 0
	v_mov_b32_e32 v86, 0
	v_mov_b32_e32 v87, 0
	v_mov_b32_e32 v88, 0
	v_mov_b32_e32 v89, 0
	ds_read2_b32 v[40:41], v92 offset0:0 offset1:152
	ds_read2_b32 v[42:43], v93 offset0:0 offset1:152
	ds_read2_b32 v[44:45], v94 offset0:0 offset1:152
	ds_read2_b32 v[46:47], v95 offset0:0 offset1:152
	ds_read2_b32 v[48:49], v96 offset0:0 offset1:152
	s_waitcnt vmcnt(36)
	v_pk_mul_f32 v[90:91], v[2:3], v[126:127]
	s_nop 0
	v_med3_f32 v90, v90, s0, v97
	v_med3_f32 v91, v91, s0, v97
	v_exp_f32_e32 v68, v90
	v_exp_f32_e32 v69, v91
	s_waitcnt lgkmcnt(0)
	ds_read2_b32 v[50:51], v92 offset0:1 offset1:153
	ds_read2_b32 v[52:53], v93 offset0:1 offset1:153
	ds_read2_b32 v[54:55], v94 offset0:1 offset1:153
	ds_read2_b32 v[56:57], v95 offset0:1 offset1:153
	ds_read2_b32 v[58:59], v96 offset0:1 offset1:153
	v_pk_add_f32 v[88:89], v[88:89], v[48:49]
	v_pk_add_f32 v[74:75], v[48:49], v[48:49]
	v_pk_fma_f32 v[60:61], v[68:69], v[40:41], v[124:125] op_sel_hi:[0,1,1]
	v_pk_fma_f32 v[62:63], v[68:69], v[42:43], v[124:125] op_sel_hi:[0,1,1]
	v_pk_fma_f32 v[64:65], v[68:69], v[44:45], v[124:125] op_sel:[1,0,0]
	v_pk_fma_f32 v[66:67], v[68:69], v[46:47], v[124:125] op_sel:[1,0,0]
	v_rcp_f32_e32 v60, v60
	v_rcp_f32_e32 v61, v61
	v_rcp_f32_e32 v62, v62
	v_rcp_f32_e32 v63, v63
	v_rcp_f32_e32 v64, v64
	v_rcp_f32_e32 v65, v65
	v_rcp_f32_e32 v66, v66
	v_rcp_f32_e32 v67, v67
	s_waitcnt vmcnt(34)
	v_pk_mul_f32 v[90:91], v[4:5], v[126:127]
	s_nop 0
	v_med3_f32 v90, v90, s0, v97
	v_med3_f32 v91, v91, s0, v97
	v_exp_f32_e32 v72, v90
	v_exp_f32_e32 v73, v91
	v_pk_fma_f32 v[80:81], v[74:75], v[60:61], v[80:81] op_sel_hi:[0,1,1] neg_lo:[1,0,0] neg_hi:[1,0,0]
	v_pk_fma_f32 v[82:83], v[74:75], v[62:63], v[82:83] op_sel_hi:[0,1,1] neg_lo:[1,0,0] neg_hi:[1,0,0]
	v_pk_fma_f32 v[84:85], v[74:75], v[64:65], v[84:85] op_sel:[1,0,0] neg_lo:[1,0,0] neg_hi:[1,0,0]
	v_pk_fma_f32 v[86:87], v[74:75], v[66:67], v[86:87] op_sel:[1,0,0] neg_lo:[1,0,0] neg_hi:[1,0,0]
	s_waitcnt lgkmcnt(0)
	ds_read2_b32 v[40:41], v92 offset0:2 offset1:154
	ds_read2_b32 v[42:43], v93 offset0:2 offset1:154
	ds_read2_b32 v[44:45], v94 offset0:2 offset1:154
	ds_read2_b32 v[46:47], v95 offset0:2 offset1:154
	ds_read2_b32 v[48:49], v96 offset0:2 offset1:154
	v_pk_add_f32 v[88:89], v[88:89], v[58:59]
	v_pk_add_f32 v[74:75], v[58:59], v[58:59]
	v_pk_fma_f32 v[60:61], v[72:73], v[50:51], v[124:125] op_sel_hi:[0,1,1]
	v_pk_fma_f32 v[62:63], v[72:73], v[52:53], v[124:125] op_sel_hi:[0,1,1]
	v_pk_fma_f32 v[64:65], v[72:73], v[54:55], v[124:125] op_sel:[1,0,0]
	v_pk_fma_f32 v[66:67], v[72:73], v[56:57], v[124:125] op_sel:[1,0,0]
	v_rcp_f32_e32 v60, v60
	v_rcp_f32_e32 v61, v61
	v_rcp_f32_e32 v62, v62
	v_rcp_f32_e32 v63, v63
	v_rcp_f32_e32 v64, v64
	v_rcp_f32_e32 v65, v65
	v_rcp_f32_e32 v66, v66
	v_rcp_f32_e32 v67, v67
	s_waitcnt vmcnt(32)
	v_pk_mul_f32 v[90:91], v[6:7], v[126:127]
	s_nop 0
	v_med3_f32 v90, v90, s0, v97
	v_med3_f32 v91, v91, s0, v97
	v_exp_f32_e32 v68, v90
	v_exp_f32_e32 v69, v91
	v_pk_fma_f32 v[80:81], v[74:75], v[60:61], v[80:81] op_sel_hi:[0,1,1] neg_lo:[1,0,0] neg_hi:[1,0,0]
	v_pk_fma_f32 v[82:83], v[74:75], v[62:63], v[82:83] op_sel_hi:[0,1,1] neg_lo:[1,0,0] neg_hi:[1,0,0]
	v_pk_fma_f32 v[84:85], v[74:75], v[64:65], v[84:85] op_sel:[1,0,0] neg_lo:[1,0,0] neg_hi:[1,0,0]
	v_pk_fma_f32 v[86:87], v[74:75], v[66:67], v[86:87] op_sel:[1,0,0] neg_lo:[1,0,0] neg_hi:[1,0,0]
	s_waitcnt lgkmcnt(0)
	ds_read2_b32 v[50:51], v92 offset0:3 offset1:155
	ds_read2_b32 v[52:53], v93 offset0:3 offset1:155
	ds_read2_b32 v[54:55], v94 offset0:3 offset1:155
	ds_read2_b32 v[56:57], v95 offset0:3 offset1:155
	ds_read2_b32 v[58:59], v96 offset0:3 offset1:155
	v_pk_add_f32 v[88:89], v[88:89], v[48:49]
	v_pk_add_f32 v[74:75], v[48:49], v[48:49]
	v_pk_fma_f32 v[60:61], v[68:69], v[40:41], v[124:125] op_sel_hi:[0,1,1]
	v_pk_fma_f32 v[62:63], v[68:69], v[42:43], v[124:125] op_sel_hi:[0,1,1]
	v_pk_fma_f32 v[64:65], v[68:69], v[44:45], v[124:125] op_sel:[1,0,0]
	v_pk_fma_f32 v[66:67], v[68:69], v[46:47], v[124:125] op_sel:[1,0,0]
	v_rcp_f32_e32 v60, v60
	v_rcp_f32_e32 v61, v61
	v_rcp_f32_e32 v62, v62
	v_rcp_f32_e32 v63, v63
	v_rcp_f32_e32 v64, v64
	v_rcp_f32_e32 v65, v65
	v_rcp_f32_e32 v66, v66
	v_rcp_f32_e32 v67, v67
	s_waitcnt vmcnt(30)
	v_pk_mul_f32 v[90:91], v[8:9], v[126:127]
	s_nop 0
	v_med3_f32 v90, v90, s0, v97
	v_med3_f32 v91, v91, s0, v97
	v_exp_f32_e32 v72, v90
	v_exp_f32_e32 v73, v91
	v_pk_fma_f32 v[80:81], v[74:75], v[60:61], v[80:81] op_sel_hi:[0,1,1] neg_lo:[1,0,0] neg_hi:[1,0,0]
	v_pk_fma_f32 v[82:83], v[74:75], v[62:63], v[82:83] op_sel_hi:[0,1,1] neg_lo:[1,0,0] neg_hi:[1,0,0]
	v_pk_fma_f32 v[84:85], v[74:75], v[64:65], v[84:85] op_sel:[1,0,0] neg_lo:[1,0,0] neg_hi:[1,0,0]
	v_pk_fma_f32 v[86:87], v[74:75], v[66:67], v[86:87] op_sel:[1,0,0] neg_lo:[1,0,0] neg_hi:[1,0,0]
	s_waitcnt lgkmcnt(0)
	ds_read2_b32 v[40:41], v92 offset0:4 offset1:156
	ds_read2_b32 v[42:43], v93 offset0:4 offset1:156
	ds_read2_b32 v[44:45], v94 offset0:4 offset1:156
	ds_read2_b32 v[46:47], v95 offset0:4 offset1:156
	ds_read2_b32 v[48:49], v96 offset0:4 offset1:156
	v_pk_add_f32 v[88:89], v[88:89], v[58:59]
	v_pk_add_f32 v[74:75], v[58:59], v[58:59]
	v_pk_fma_f32 v[60:61], v[72:73], v[50:51], v[124:125] op_sel_hi:[0,1,1]
	v_pk_fma_f32 v[62:63], v[72:73], v[52:53], v[124:125] op_sel_hi:[0,1,1]
	v_pk_fma_f32 v[64:65], v[72:73], v[54:55], v[124:125] op_sel:[1,0,0]
	v_pk_fma_f32 v[66:67], v[72:73], v[56:57], v[124:125] op_sel:[1,0,0]
	v_rcp_f32_e32 v60, v60
	v_rcp_f32_e32 v61, v61
	v_rcp_f32_e32 v62, v62
	v_rcp_f32_e32 v63, v63
	v_rcp_f32_e32 v64, v64
	v_rcp_f32_e32 v65, v65
	v_rcp_f32_e32 v66, v66
	v_rcp_f32_e32 v67, v67
	s_waitcnt vmcnt(28)
	v_pk_mul_f32 v[90:91], v[10:11], v[126:127]
	s_nop 0
	v_med3_f32 v90, v90, s0, v97
	v_med3_f32 v91, v91, s0, v97
	v_exp_f32_e32 v68, v90
	v_exp_f32_e32 v69, v91
	v_pk_fma_f32 v[80:81], v[74:75], v[60:61], v[80:81] op_sel_hi:[0,1,1] neg_lo:[1,0,0] neg_hi:[1,0,0]
	v_pk_fma_f32 v[82:83], v[74:75], v[62:63], v[82:83] op_sel_hi:[0,1,1] neg_lo:[1,0,0] neg_hi:[1,0,0]
	v_pk_fma_f32 v[84:85], v[74:75], v[64:65], v[84:85] op_sel:[1,0,0] neg_lo:[1,0,0] neg_hi:[1,0,0]
	v_pk_fma_f32 v[86:87], v[74:75], v[66:67], v[86:87] op_sel:[1,0,0] neg_lo:[1,0,0] neg_hi:[1,0,0]
	s_waitcnt lgkmcnt(0)
	ds_read2_b32 v[50:51], v92 offset0:5 offset1:157
	ds_read2_b32 v[52:53], v93 offset0:5 offset1:157
	ds_read2_b32 v[54:55], v94 offset0:5 offset1:157
	ds_read2_b32 v[56:57], v95 offset0:5 offset1:157
	ds_read2_b32 v[58:59], v96 offset0:5 offset1:157
	v_pk_add_f32 v[88:89], v[88:89], v[48:49]
	v_pk_add_f32 v[74:75], v[48:49], v[48:49]
	v_pk_fma_f32 v[60:61], v[68:69], v[40:41], v[124:125] op_sel_hi:[0,1,1]
	v_pk_fma_f32 v[62:63], v[68:69], v[42:43], v[124:125] op_sel_hi:[0,1,1]
	v_pk_fma_f32 v[64:65], v[68:69], v[44:45], v[124:125] op_sel:[1,0,0]
	v_pk_fma_f32 v[66:67], v[68:69], v[46:47], v[124:125] op_sel:[1,0,0]
	v_rcp_f32_e32 v60, v60
	v_rcp_f32_e32 v61, v61
	v_rcp_f32_e32 v62, v62
	v_rcp_f32_e32 v63, v63
	v_rcp_f32_e32 v64, v64
	v_rcp_f32_e32 v65, v65
	v_rcp_f32_e32 v66, v66
	v_rcp_f32_e32 v67, v67
	s_waitcnt vmcnt(26)
	v_pk_mul_f32 v[90:91], v[12:13], v[126:127]
	s_nop 0
	v_med3_f32 v90, v90, s0, v97
	v_med3_f32 v91, v91, s0, v97
	v_exp_f32_e32 v72, v90
	v_exp_f32_e32 v73, v91
	v_pk_fma_f32 v[80:81], v[74:75], v[60:61], v[80:81] op_sel_hi:[0,1,1] neg_lo:[1,0,0] neg_hi:[1,0,0]
	v_pk_fma_f32 v[82:83], v[74:75], v[62:63], v[82:83] op_sel_hi:[0,1,1] neg_lo:[1,0,0] neg_hi:[1,0,0]
	v_pk_fma_f32 v[84:85], v[74:75], v[64:65], v[84:85] op_sel:[1,0,0] neg_lo:[1,0,0] neg_hi:[1,0,0]
	v_pk_fma_f32 v[86:87], v[74:75], v[66:67], v[86:87] op_sel:[1,0,0] neg_lo:[1,0,0] neg_hi:[1,0,0]
	s_waitcnt lgkmcnt(0)
	ds_read2_b32 v[40:41], v92 offset0:6 offset1:158
	ds_read2_b32 v[42:43], v93 offset0:6 offset1:158
	ds_read2_b32 v[44:45], v94 offset0:6 offset1:158
	ds_read2_b32 v[46:47], v95 offset0:6 offset1:158
	ds_read2_b32 v[48:49], v96 offset0:6 offset1:158
	v_pk_add_f32 v[88:89], v[88:89], v[58:59]
	v_pk_add_f32 v[74:75], v[58:59], v[58:59]
	v_pk_fma_f32 v[60:61], v[72:73], v[50:51], v[124:125] op_sel_hi:[0,1,1]
	v_pk_fma_f32 v[62:63], v[72:73], v[52:53], v[124:125] op_sel_hi:[0,1,1]
	v_pk_fma_f32 v[64:65], v[72:73], v[54:55], v[124:125] op_sel:[1,0,0]
	v_pk_fma_f32 v[66:67], v[72:73], v[56:57], v[124:125] op_sel:[1,0,0]
	v_rcp_f32_e32 v60, v60
	v_rcp_f32_e32 v61, v61
	v_rcp_f32_e32 v62, v62
	v_rcp_f32_e32 v63, v63
	v_rcp_f32_e32 v64, v64
	v_rcp_f32_e32 v65, v65
	v_rcp_f32_e32 v66, v66
	v_rcp_f32_e32 v67, v67
	s_waitcnt vmcnt(24)
	v_pk_mul_f32 v[90:91], v[14:15], v[126:127]
	s_nop 0
	v_med3_f32 v90, v90, s0, v97
	v_med3_f32 v91, v91, s0, v97
	v_exp_f32_e32 v68, v90
	v_exp_f32_e32 v69, v91
	v_pk_fma_f32 v[80:81], v[74:75], v[60:61], v[80:81] op_sel_hi:[0,1,1] neg_lo:[1,0,0] neg_hi:[1,0,0]
	v_pk_fma_f32 v[82:83], v[74:75], v[62:63], v[82:83] op_sel_hi:[0,1,1] neg_lo:[1,0,0] neg_hi:[1,0,0]
	v_pk_fma_f32 v[84:85], v[74:75], v[64:65], v[84:85] op_sel:[1,0,0] neg_lo:[1,0,0] neg_hi:[1,0,0]
	v_pk_fma_f32 v[86:87], v[74:75], v[66:67], v[86:87] op_sel:[1,0,0] neg_lo:[1,0,0] neg_hi:[1,0,0]
	s_waitcnt lgkmcnt(0)
	ds_read2_b32 v[50:51], v92 offset0:7 offset1:159
	ds_read2_b32 v[52:53], v93 offset0:7 offset1:159
	ds_read2_b32 v[54:55], v94 offset0:7 offset1:159
	ds_read2_b32 v[56:57], v95 offset0:7 offset1:159
	ds_read2_b32 v[58:59], v96 offset0:7 offset1:159
	v_pk_add_f32 v[88:89], v[88:89], v[48:49]
	v_pk_add_f32 v[74:75], v[48:49], v[48:49]
	v_pk_fma_f32 v[60:61], v[68:69], v[40:41], v[124:125] op_sel_hi:[0,1,1]
	v_pk_fma_f32 v[62:63], v[68:69], v[42:43], v[124:125] op_sel_hi:[0,1,1]
	v_pk_fma_f32 v[64:65], v[68:69], v[44:45], v[124:125] op_sel:[1,0,0]
	v_pk_fma_f32 v[66:67], v[68:69], v[46:47], v[124:125] op_sel:[1,0,0]
	v_rcp_f32_e32 v60, v60
	v_rcp_f32_e32 v61, v61
	v_rcp_f32_e32 v62, v62
	v_rcp_f32_e32 v63, v63
	v_rcp_f32_e32 v64, v64
	v_rcp_f32_e32 v65, v65
	v_rcp_f32_e32 v66, v66
	v_rcp_f32_e32 v67, v67
	s_waitcnt vmcnt(22)
	v_pk_mul_f32 v[90:91], v[16:17], v[126:127]
	s_nop 0
	v_med3_f32 v90, v90, s0, v97
	v_med3_f32 v91, v91, s0, v97
	v_exp_f32_e32 v72, v90
	v_exp_f32_e32 v73, v91
	v_pk_fma_f32 v[80:81], v[74:75], v[60:61], v[80:81] op_sel_hi:[0,1,1] neg_lo:[1,0,0] neg_hi:[1,0,0]
	v_pk_fma_f32 v[82:83], v[74:75], v[62:63], v[82:83] op_sel_hi:[0,1,1] neg_lo:[1,0,0] neg_hi:[1,0,0]
	v_pk_fma_f32 v[84:85], v[74:75], v[64:65], v[84:85] op_sel:[1,0,0] neg_lo:[1,0,0] neg_hi:[1,0,0]
	v_pk_fma_f32 v[86:87], v[74:75], v[66:67], v[86:87] op_sel:[1,0,0] neg_lo:[1,0,0] neg_hi:[1,0,0]
	s_waitcnt lgkmcnt(0)
	ds_read2_b32 v[40:41], v92 offset0:8 offset1:160
	ds_read2_b32 v[42:43], v93 offset0:8 offset1:160
	ds_read2_b32 v[44:45], v94 offset0:8 offset1:160
	ds_read2_b32 v[46:47], v95 offset0:8 offset1:160
	ds_read2_b32 v[48:49], v96 offset0:8 offset1:160
	v_pk_add_f32 v[88:89], v[88:89], v[58:59]
	v_pk_add_f32 v[74:75], v[58:59], v[58:59]
	v_pk_fma_f32 v[60:61], v[72:73], v[50:51], v[124:125] op_sel_hi:[0,1,1]
	v_pk_fma_f32 v[62:63], v[72:73], v[52:53], v[124:125] op_sel_hi:[0,1,1]
	v_pk_fma_f32 v[64:65], v[72:73], v[54:55], v[124:125] op_sel:[1,0,0]
	v_pk_fma_f32 v[66:67], v[72:73], v[56:57], v[124:125] op_sel:[1,0,0]
	v_rcp_f32_e32 v60, v60
	v_rcp_f32_e32 v61, v61
	v_rcp_f32_e32 v62, v62
	v_rcp_f32_e32 v63, v63
	v_rcp_f32_e32 v64, v64
	v_rcp_f32_e32 v65, v65
	v_rcp_f32_e32 v66, v66
	v_rcp_f32_e32 v67, v67
	s_waitcnt vmcnt(20)
	v_pk_mul_f32 v[90:91], v[18:19], v[126:127]
	s_nop 0
	v_med3_f32 v90, v90, s0, v97
	v_med3_f32 v91, v91, s0, v97
	v_exp_f32_e32 v68, v90
	v_exp_f32_e32 v69, v91
	v_pk_fma_f32 v[80:81], v[74:75], v[60:61], v[80:81] op_sel_hi:[0,1,1] neg_lo:[1,0,0] neg_hi:[1,0,0]
	v_pk_fma_f32 v[82:83], v[74:75], v[62:63], v[82:83] op_sel_hi:[0,1,1] neg_lo:[1,0,0] neg_hi:[1,0,0]
	v_pk_fma_f32 v[84:85], v[74:75], v[64:65], v[84:85] op_sel:[1,0,0] neg_lo:[1,0,0] neg_hi:[1,0,0]
	v_pk_fma_f32 v[86:87], v[74:75], v[66:67], v[86:87] op_sel:[1,0,0] neg_lo:[1,0,0] neg_hi:[1,0,0]
	s_waitcnt lgkmcnt(0)
	ds_read2_b32 v[50:51], v92 offset0:9 offset1:161
	ds_read2_b32 v[52:53], v93 offset0:9 offset1:161
	ds_read2_b32 v[54:55], v94 offset0:9 offset1:161
	ds_read2_b32 v[56:57], v95 offset0:9 offset1:161
	ds_read2_b32 v[58:59], v96 offset0:9 offset1:161
	v_pk_add_f32 v[88:89], v[88:89], v[48:49]
	v_pk_add_f32 v[74:75], v[48:49], v[48:49]
	v_pk_fma_f32 v[60:61], v[68:69], v[40:41], v[124:125] op_sel_hi:[0,1,1]
	v_pk_fma_f32 v[62:63], v[68:69], v[42:43], v[124:125] op_sel_hi:[0,1,1]
	v_pk_fma_f32 v[64:65], v[68:69], v[44:45], v[124:125] op_sel:[1,0,0]
	v_pk_fma_f32 v[66:67], v[68:69], v[46:47], v[124:125] op_sel:[1,0,0]
	v_rcp_f32_e32 v60, v60
	v_rcp_f32_e32 v61, v61
	v_rcp_f32_e32 v62, v62
	v_rcp_f32_e32 v63, v63
	v_rcp_f32_e32 v64, v64
	v_rcp_f32_e32 v65, v65
	v_rcp_f32_e32 v66, v66
	v_rcp_f32_e32 v67, v67
	s_waitcnt vmcnt(18)
	v_pk_mul_f32 v[90:91], v[20:21], v[126:127]
	s_nop 0
	v_med3_f32 v90, v90, s0, v97
	v_med3_f32 v91, v91, s0, v97
	v_exp_f32_e32 v72, v90
	v_exp_f32_e32 v73, v91
	v_pk_fma_f32 v[80:81], v[74:75], v[60:61], v[80:81] op_sel_hi:[0,1,1] neg_lo:[1,0,0] neg_hi:[1,0,0]
	v_pk_fma_f32 v[82:83], v[74:75], v[62:63], v[82:83] op_sel_hi:[0,1,1] neg_lo:[1,0,0] neg_hi:[1,0,0]
	v_pk_fma_f32 v[84:85], v[74:75], v[64:65], v[84:85] op_sel:[1,0,0] neg_lo:[1,0,0] neg_hi:[1,0,0]
	v_pk_fma_f32 v[86:87], v[74:75], v[66:67], v[86:87] op_sel:[1,0,0] neg_lo:[1,0,0] neg_hi:[1,0,0]
	s_waitcnt lgkmcnt(0)
	ds_read2_b32 v[40:41], v92 offset0:10 offset1:162
	ds_read2_b32 v[42:43], v93 offset0:10 offset1:162
	ds_read2_b32 v[44:45], v94 offset0:10 offset1:162
	ds_read2_b32 v[46:47], v95 offset0:10 offset1:162
	ds_read2_b32 v[48:49], v96 offset0:10 offset1:162
	v_pk_add_f32 v[88:89], v[88:89], v[58:59]
	v_pk_add_f32 v[74:75], v[58:59], v[58:59]
	v_pk_fma_f32 v[60:61], v[72:73], v[50:51], v[124:125] op_sel_hi:[0,1,1]
	v_pk_fma_f32 v[62:63], v[72:73], v[52:53], v[124:125] op_sel_hi:[0,1,1]
	v_pk_fma_f32 v[64:65], v[72:73], v[54:55], v[124:125] op_sel:[1,0,0]
	v_pk_fma_f32 v[66:67], v[72:73], v[56:57], v[124:125] op_sel:[1,0,0]
	v_rcp_f32_e32 v60, v60
	v_rcp_f32_e32 v61, v61
	v_rcp_f32_e32 v62, v62
	v_rcp_f32_e32 v63, v63
	v_rcp_f32_e32 v64, v64
	v_rcp_f32_e32 v65, v65
	v_rcp_f32_e32 v66, v66
	v_rcp_f32_e32 v67, v67
	s_waitcnt vmcnt(16)
	v_pk_mul_f32 v[90:91], v[22:23], v[126:127]
	s_nop 0
	v_med3_f32 v90, v90, s0, v97
	v_med3_f32 v91, v91, s0, v97
	v_exp_f32_e32 v68, v90
	v_exp_f32_e32 v69, v91
	v_pk_fma_f32 v[80:81], v[74:75], v[60:61], v[80:81] op_sel_hi:[0,1,1] neg_lo:[1,0,0] neg_hi:[1,0,0]
	v_pk_fma_f32 v[82:83], v[74:75], v[62:63], v[82:83] op_sel_hi:[0,1,1] neg_lo:[1,0,0] neg_hi:[1,0,0]
	v_pk_fma_f32 v[84:85], v[74:75], v[64:65], v[84:85] op_sel:[1,0,0] neg_lo:[1,0,0] neg_hi:[1,0,0]
	v_pk_fma_f32 v[86:87], v[74:75], v[66:67], v[86:87] op_sel:[1,0,0] neg_lo:[1,0,0] neg_hi:[1,0,0]
	s_waitcnt lgkmcnt(0)
	ds_read2_b32 v[50:51], v92 offset0:11 offset1:163
	ds_read2_b32 v[52:53], v93 offset0:11 offset1:163
	ds_read2_b32 v[54:55], v94 offset0:11 offset1:163
	ds_read2_b32 v[56:57], v95 offset0:11 offset1:163
	ds_read2_b32 v[58:59], v96 offset0:11 offset1:163
	v_pk_add_f32 v[88:89], v[88:89], v[48:49]
	v_pk_add_f32 v[74:75], v[48:49], v[48:49]
	v_pk_fma_f32 v[60:61], v[68:69], v[40:41], v[124:125] op_sel_hi:[0,1,1]
	v_pk_fma_f32 v[62:63], v[68:69], v[42:43], v[124:125] op_sel_hi:[0,1,1]
	v_pk_fma_f32 v[64:65], v[68:69], v[44:45], v[124:125] op_sel:[1,0,0]
	v_pk_fma_f32 v[66:67], v[68:69], v[46:47], v[124:125] op_sel:[1,0,0]
	v_rcp_f32_e32 v60, v60
	v_rcp_f32_e32 v61, v61
	v_rcp_f32_e32 v62, v62
	v_rcp_f32_e32 v63, v63
	v_rcp_f32_e32 v64, v64
	v_rcp_f32_e32 v65, v65
	v_rcp_f32_e32 v66, v66
	v_rcp_f32_e32 v67, v67
	s_waitcnt vmcnt(14)
	v_pk_mul_f32 v[90:91], v[24:25], v[126:127]
	s_nop 0
	v_med3_f32 v90, v90, s0, v97
	v_med3_f32 v91, v91, s0, v97
	v_exp_f32_e32 v72, v90
	v_exp_f32_e32 v73, v91
	v_pk_fma_f32 v[80:81], v[74:75], v[60:61], v[80:81] op_sel_hi:[0,1,1] neg_lo:[1,0,0] neg_hi:[1,0,0]
	v_pk_fma_f32 v[82:83], v[74:75], v[62:63], v[82:83] op_sel_hi:[0,1,1] neg_lo:[1,0,0] neg_hi:[1,0,0]
	v_pk_fma_f32 v[84:85], v[74:75], v[64:65], v[84:85] op_sel:[1,0,0] neg_lo:[1,0,0] neg_hi:[1,0,0]
	v_pk_fma_f32 v[86:87], v[74:75], v[66:67], v[86:87] op_sel:[1,0,0] neg_lo:[1,0,0] neg_hi:[1,0,0]
	s_waitcnt lgkmcnt(0)
	ds_read2_b32 v[40:41], v92 offset0:12 offset1:164
	ds_read2_b32 v[42:43], v93 offset0:12 offset1:164
	ds_read2_b32 v[44:45], v94 offset0:12 offset1:164
	ds_read2_b32 v[46:47], v95 offset0:12 offset1:164
	ds_read2_b32 v[48:49], v96 offset0:12 offset1:164
	v_pk_add_f32 v[88:89], v[88:89], v[58:59]
	v_pk_add_f32 v[74:75], v[58:59], v[58:59]
	v_pk_fma_f32 v[60:61], v[72:73], v[50:51], v[124:125] op_sel_hi:[0,1,1]
	v_pk_fma_f32 v[62:63], v[72:73], v[52:53], v[124:125] op_sel_hi:[0,1,1]
	v_pk_fma_f32 v[64:65], v[72:73], v[54:55], v[124:125] op_sel:[1,0,0]
	v_pk_fma_f32 v[66:67], v[72:73], v[56:57], v[124:125] op_sel:[1,0,0]
	v_rcp_f32_e32 v60, v60
	v_rcp_f32_e32 v61, v61
	v_rcp_f32_e32 v62, v62
	v_rcp_f32_e32 v63, v63
	v_rcp_f32_e32 v64, v64
	v_rcp_f32_e32 v65, v65
	v_rcp_f32_e32 v66, v66
	v_rcp_f32_e32 v67, v67
	s_waitcnt vmcnt(12)
	v_pk_mul_f32 v[90:91], v[26:27], v[126:127]
	s_nop 0
	v_med3_f32 v90, v90, s0, v97
	v_med3_f32 v91, v91, s0, v97
	v_exp_f32_e32 v68, v90
	v_exp_f32_e32 v69, v91
	v_pk_fma_f32 v[80:81], v[74:75], v[60:61], v[80:81] op_sel_hi:[0,1,1] neg_lo:[1,0,0] neg_hi:[1,0,0]
	v_pk_fma_f32 v[82:83], v[74:75], v[62:63], v[82:83] op_sel_hi:[0,1,1] neg_lo:[1,0,0] neg_hi:[1,0,0]
	v_pk_fma_f32 v[84:85], v[74:75], v[64:65], v[84:85] op_sel:[1,0,0] neg_lo:[1,0,0] neg_hi:[1,0,0]
	v_pk_fma_f32 v[86:87], v[74:75], v[66:67], v[86:87] op_sel:[1,0,0] neg_lo:[1,0,0] neg_hi:[1,0,0]
	s_waitcnt lgkmcnt(0)
	ds_read2_b32 v[50:51], v92 offset0:13 offset1:165
	ds_read2_b32 v[52:53], v93 offset0:13 offset1:165
	ds_read2_b32 v[54:55], v94 offset0:13 offset1:165
	ds_read2_b32 v[56:57], v95 offset0:13 offset1:165
	ds_read2_b32 v[58:59], v96 offset0:13 offset1:165
	v_pk_add_f32 v[88:89], v[88:89], v[48:49]
	v_pk_add_f32 v[74:75], v[48:49], v[48:49]
	v_pk_fma_f32 v[60:61], v[68:69], v[40:41], v[124:125] op_sel_hi:[0,1,1]
	v_pk_fma_f32 v[62:63], v[68:69], v[42:43], v[124:125] op_sel_hi:[0,1,1]
	v_pk_fma_f32 v[64:65], v[68:69], v[44:45], v[124:125] op_sel:[1,0,0]
	v_pk_fma_f32 v[66:67], v[68:69], v[46:47], v[124:125] op_sel:[1,0,0]
	v_rcp_f32_e32 v60, v60
	v_rcp_f32_e32 v61, v61
	v_rcp_f32_e32 v62, v62
	v_rcp_f32_e32 v63, v63
	v_rcp_f32_e32 v64, v64
	v_rcp_f32_e32 v65, v65
	v_rcp_f32_e32 v66, v66
	v_rcp_f32_e32 v67, v67
	s_waitcnt vmcnt(10)
	v_pk_mul_f32 v[90:91], v[28:29], v[126:127]
	s_nop 0
	v_med3_f32 v90, v90, s0, v97
	v_med3_f32 v91, v91, s0, v97
	v_exp_f32_e32 v72, v90
	v_exp_f32_e32 v73, v91
	v_pk_fma_f32 v[80:81], v[74:75], v[60:61], v[80:81] op_sel_hi:[0,1,1] neg_lo:[1,0,0] neg_hi:[1,0,0]
	v_pk_fma_f32 v[82:83], v[74:75], v[62:63], v[82:83] op_sel_hi:[0,1,1] neg_lo:[1,0,0] neg_hi:[1,0,0]
	v_pk_fma_f32 v[84:85], v[74:75], v[64:65], v[84:85] op_sel:[1,0,0] neg_lo:[1,0,0] neg_hi:[1,0,0]
	v_pk_fma_f32 v[86:87], v[74:75], v[66:67], v[86:87] op_sel:[1,0,0] neg_lo:[1,0,0] neg_hi:[1,0,0]
	s_waitcnt lgkmcnt(0)
	ds_read2_b32 v[40:41], v92 offset0:14 offset1:166
	ds_read2_b32 v[42:43], v93 offset0:14 offset1:166
	ds_read2_b32 v[44:45], v94 offset0:14 offset1:166
	ds_read2_b32 v[46:47], v95 offset0:14 offset1:166
	ds_read2_b32 v[48:49], v96 offset0:14 offset1:166
	v_pk_add_f32 v[88:89], v[88:89], v[58:59]
	v_pk_add_f32 v[74:75], v[58:59], v[58:59]
	v_pk_fma_f32 v[60:61], v[72:73], v[50:51], v[124:125] op_sel_hi:[0,1,1]
	v_pk_fma_f32 v[62:63], v[72:73], v[52:53], v[124:125] op_sel_hi:[0,1,1]
	v_pk_fma_f32 v[64:65], v[72:73], v[54:55], v[124:125] op_sel:[1,0,0]
	v_pk_fma_f32 v[66:67], v[72:73], v[56:57], v[124:125] op_sel:[1,0,0]
	v_rcp_f32_e32 v60, v60
	v_rcp_f32_e32 v61, v61
	v_rcp_f32_e32 v62, v62
	v_rcp_f32_e32 v63, v63
	v_rcp_f32_e32 v64, v64
	v_rcp_f32_e32 v65, v65
	v_rcp_f32_e32 v66, v66
	v_rcp_f32_e32 v67, v67
	s_waitcnt vmcnt(8)
	v_pk_mul_f32 v[90:91], v[30:31], v[126:127]
	s_nop 0
	v_med3_f32 v90, v90, s0, v97
	v_med3_f32 v91, v91, s0, v97
	v_exp_f32_e32 v68, v90
	v_exp_f32_e32 v69, v91
	v_pk_fma_f32 v[80:81], v[74:75], v[60:61], v[80:81] op_sel_hi:[0,1,1] neg_lo:[1,0,0] neg_hi:[1,0,0]
	v_pk_fma_f32 v[82:83], v[74:75], v[62:63], v[82:83] op_sel_hi:[0,1,1] neg_lo:[1,0,0] neg_hi:[1,0,0]
	v_pk_fma_f32 v[84:85], v[74:75], v[64:65], v[84:85] op_sel:[1,0,0] neg_lo:[1,0,0] neg_hi:[1,0,0]
	v_pk_fma_f32 v[86:87], v[74:75], v[66:67], v[86:87] op_sel:[1,0,0] neg_lo:[1,0,0] neg_hi:[1,0,0]
	s_waitcnt lgkmcnt(0)
	ds_read2_b32 v[50:51], v92 offset0:15 offset1:167
	ds_read2_b32 v[52:53], v93 offset0:15 offset1:167
	ds_read2_b32 v[54:55], v94 offset0:15 offset1:167
	ds_read2_b32 v[56:57], v95 offset0:15 offset1:167
	ds_read2_b32 v[58:59], v96 offset0:15 offset1:167
	v_pk_add_f32 v[88:89], v[88:89], v[48:49]
	v_pk_add_f32 v[74:75], v[48:49], v[48:49]
	v_pk_fma_f32 v[60:61], v[68:69], v[40:41], v[124:125] op_sel_hi:[0,1,1]
	v_pk_fma_f32 v[62:63], v[68:69], v[42:43], v[124:125] op_sel_hi:[0,1,1]
	v_pk_fma_f32 v[64:65], v[68:69], v[44:45], v[124:125] op_sel:[1,0,0]
	v_pk_fma_f32 v[66:67], v[68:69], v[46:47], v[124:125] op_sel:[1,0,0]
	v_rcp_f32_e32 v60, v60
	v_rcp_f32_e32 v61, v61
	v_rcp_f32_e32 v62, v62
	v_rcp_f32_e32 v63, v63
	v_rcp_f32_e32 v64, v64
	v_rcp_f32_e32 v65, v65
	v_rcp_f32_e32 v66, v66
	v_rcp_f32_e32 v67, v67
	s_waitcnt vmcnt(6)
	v_pk_mul_f32 v[90:91], v[32:33], v[126:127]
	s_nop 0
	v_med3_f32 v90, v90, s0, v97
	v_med3_f32 v91, v91, s0, v97
	v_exp_f32_e32 v72, v90
	v_exp_f32_e32 v73, v91
	v_pk_fma_f32 v[80:81], v[74:75], v[60:61], v[80:81] op_sel_hi:[0,1,1] neg_lo:[1,0,0] neg_hi:[1,0,0]
	v_pk_fma_f32 v[82:83], v[74:75], v[62:63], v[82:83] op_sel_hi:[0,1,1] neg_lo:[1,0,0] neg_hi:[1,0,0]
	v_pk_fma_f32 v[84:85], v[74:75], v[64:65], v[84:85] op_sel:[1,0,0] neg_lo:[1,0,0] neg_hi:[1,0,0]
	v_pk_fma_f32 v[86:87], v[74:75], v[66:67], v[86:87] op_sel:[1,0,0] neg_lo:[1,0,0] neg_hi:[1,0,0]
	s_waitcnt lgkmcnt(0)
	ds_read2_b32 v[40:41], v92 offset0:16 offset1:168
	ds_read2_b32 v[42:43], v93 offset0:16 offset1:168
	ds_read2_b32 v[44:45], v94 offset0:16 offset1:168
	ds_read2_b32 v[46:47], v95 offset0:16 offset1:168
	ds_read2_b32 v[48:49], v96 offset0:16 offset1:168
	v_pk_add_f32 v[88:89], v[88:89], v[58:59]
	v_pk_add_f32 v[74:75], v[58:59], v[58:59]
	v_pk_fma_f32 v[60:61], v[72:73], v[50:51], v[124:125] op_sel_hi:[0,1,1]
	v_pk_fma_f32 v[62:63], v[72:73], v[52:53], v[124:125] op_sel_hi:[0,1,1]
	v_pk_fma_f32 v[64:65], v[72:73], v[54:55], v[124:125] op_sel:[1,0,0]
	v_pk_fma_f32 v[66:67], v[72:73], v[56:57], v[124:125] op_sel:[1,0,0]
	v_rcp_f32_e32 v60, v60
	v_rcp_f32_e32 v61, v61
	v_rcp_f32_e32 v62, v62
	v_rcp_f32_e32 v63, v63
	v_rcp_f32_e32 v64, v64
	v_rcp_f32_e32 v65, v65
	v_rcp_f32_e32 v66, v66
	v_rcp_f32_e32 v67, v67
	s_waitcnt vmcnt(4)
	v_pk_mul_f32 v[90:91], v[34:35], v[126:127]
	s_nop 0
	v_med3_f32 v90, v90, s0, v97
	v_med3_f32 v91, v91, s0, v97
	v_exp_f32_e32 v68, v90
	v_exp_f32_e32 v69, v91
	v_pk_fma_f32 v[80:81], v[74:75], v[60:61], v[80:81] op_sel_hi:[0,1,1] neg_lo:[1,0,0] neg_hi:[1,0,0]
	v_pk_fma_f32 v[82:83], v[74:75], v[62:63], v[82:83] op_sel_hi:[0,1,1] neg_lo:[1,0,0] neg_hi:[1,0,0]
	v_pk_fma_f32 v[84:85], v[74:75], v[64:65], v[84:85] op_sel:[1,0,0] neg_lo:[1,0,0] neg_hi:[1,0,0]
	v_pk_fma_f32 v[86:87], v[74:75], v[66:67], v[86:87] op_sel:[1,0,0] neg_lo:[1,0,0] neg_hi:[1,0,0]
	s_waitcnt lgkmcnt(0)
	ds_read2_b32 v[50:51], v92 offset0:17 offset1:169
	ds_read2_b32 v[52:53], v93 offset0:17 offset1:169
	ds_read2_b32 v[54:55], v94 offset0:17 offset1:169
	ds_read2_b32 v[56:57], v95 offset0:17 offset1:169
	ds_read2_b32 v[58:59], v96 offset0:17 offset1:169
	v_pk_add_f32 v[88:89], v[88:89], v[48:49]
	v_pk_add_f32 v[74:75], v[48:49], v[48:49]
	v_pk_fma_f32 v[60:61], v[68:69], v[40:41], v[124:125] op_sel_hi:[0,1,1]
	v_pk_fma_f32 v[62:63], v[68:69], v[42:43], v[124:125] op_sel_hi:[0,1,1]
	v_pk_fma_f32 v[64:65], v[68:69], v[44:45], v[124:125] op_sel:[1,0,0]
	v_pk_fma_f32 v[66:67], v[68:69], v[46:47], v[124:125] op_sel:[1,0,0]
	v_rcp_f32_e32 v60, v60
	v_rcp_f32_e32 v61, v61
	v_rcp_f32_e32 v62, v62
	v_rcp_f32_e32 v63, v63
	v_rcp_f32_e32 v64, v64
	v_rcp_f32_e32 v65, v65
	v_rcp_f32_e32 v66, v66
	v_rcp_f32_e32 v67, v67
	s_waitcnt vmcnt(2)
	v_pk_mul_f32 v[90:91], v[36:37], v[126:127]
	s_nop 0
	v_med3_f32 v90, v90, s0, v97
	v_med3_f32 v91, v91, s0, v97
	v_exp_f32_e32 v72, v90
	v_exp_f32_e32 v73, v91
	v_pk_fma_f32 v[80:81], v[74:75], v[60:61], v[80:81] op_sel_hi:[0,1,1] neg_lo:[1,0,0] neg_hi:[1,0,0]
	v_pk_fma_f32 v[82:83], v[74:75], v[62:63], v[82:83] op_sel_hi:[0,1,1] neg_lo:[1,0,0] neg_hi:[1,0,0]
	v_pk_fma_f32 v[84:85], v[74:75], v[64:65], v[84:85] op_sel:[1,0,0] neg_lo:[1,0,0] neg_hi:[1,0,0]
	v_pk_fma_f32 v[86:87], v[74:75], v[66:67], v[86:87] op_sel:[1,0,0] neg_lo:[1,0,0] neg_hi:[1,0,0]
	s_waitcnt lgkmcnt(0)
	ds_read2_b32 v[40:41], v92 offset0:18 offset1:170
	ds_read2_b32 v[42:43], v93 offset0:18 offset1:170
	ds_read2_b32 v[44:45], v94 offset0:18 offset1:170
	ds_read2_b32 v[46:47], v95 offset0:18 offset1:170
	ds_read2_b32 v[48:49], v96 offset0:18 offset1:170
	v_pk_add_f32 v[88:89], v[88:89], v[58:59]
	v_pk_add_f32 v[74:75], v[58:59], v[58:59]
	v_pk_fma_f32 v[60:61], v[72:73], v[50:51], v[124:125] op_sel_hi:[0,1,1]
	v_pk_fma_f32 v[62:63], v[72:73], v[52:53], v[124:125] op_sel_hi:[0,1,1]
	v_pk_fma_f32 v[64:65], v[72:73], v[54:55], v[124:125] op_sel:[1,0,0]
	v_pk_fma_f32 v[66:67], v[72:73], v[56:57], v[124:125] op_sel:[1,0,0]
	v_rcp_f32_e32 v60, v60
	v_rcp_f32_e32 v61, v61
	v_rcp_f32_e32 v62, v62
	v_rcp_f32_e32 v63, v63
	v_rcp_f32_e32 v64, v64
	v_rcp_f32_e32 v65, v65
	v_rcp_f32_e32 v66, v66
	v_rcp_f32_e32 v67, v67
	s_waitcnt vmcnt(0)
	v_pk_mul_f32 v[90:91], v[118:119], v[126:127]
	s_nop 0
	v_med3_f32 v90, v90, s0, v97
	v_med3_f32 v91, v91, s0, v97
	v_exp_f32_e32 v68, v90
	v_exp_f32_e32 v69, v91
	v_pk_fma_f32 v[80:81], v[74:75], v[60:61], v[80:81] op_sel_hi:[0,1,1] neg_lo:[1,0,0] neg_hi:[1,0,0]
	v_pk_fma_f32 v[82:83], v[74:75], v[62:63], v[82:83] op_sel_hi:[0,1,1] neg_lo:[1,0,0] neg_hi:[1,0,0]
	v_pk_fma_f32 v[84:85], v[74:75], v[64:65], v[84:85] op_sel:[1,0,0] neg_lo:[1,0,0] neg_hi:[1,0,0]
	v_pk_fma_f32 v[86:87], v[74:75], v[66:67], v[86:87] op_sel:[1,0,0] neg_lo:[1,0,0] neg_hi:[1,0,0]
	s_waitcnt lgkmcnt(0)
	v_pk_add_f32 v[88:89], v[88:89], v[48:49]
	v_pk_add_f32 v[74:75], v[48:49], v[48:49]
	v_pk_fma_f32 v[60:61], v[68:69], v[40:41], v[124:125] op_sel_hi:[0,1,1]
	v_pk_fma_f32 v[62:63], v[68:69], v[42:43], v[124:125] op_sel_hi:[0,1,1]
	v_pk_fma_f32 v[64:65], v[68:69], v[44:45], v[124:125] op_sel:[1,0,0]
	v_pk_fma_f32 v[66:67], v[68:69], v[46:47], v[124:125] op_sel:[1,0,0]
	v_rcp_f32_e32 v60, v60
	v_rcp_f32_e32 v61, v61
	v_rcp_f32_e32 v62, v62
	v_rcp_f32_e32 v63, v63
	v_rcp_f32_e32 v64, v64
	v_rcp_f32_e32 v65, v65
	v_rcp_f32_e32 v66, v66
	v_rcp_f32_e32 v67, v67
	s_nop 0
	v_pk_fma_f32 v[80:81], v[74:75], v[60:61], v[80:81] op_sel_hi:[0,1,1] neg_lo:[1,0,0] neg_hi:[1,0,0]
	v_pk_fma_f32 v[82:83], v[74:75], v[62:63], v[82:83] op_sel_hi:[0,1,1] neg_lo:[1,0,0] neg_hi:[1,0,0]
	v_pk_fma_f32 v[84:85], v[74:75], v[64:65], v[84:85] op_sel:[1,0,0] neg_lo:[1,0,0] neg_hi:[1,0,0]
	v_pk_fma_f32 v[86:87], v[74:75], v[66:67], v[86:87] op_sel:[1,0,0] neg_lo:[1,0,0] neg_hi:[1,0,0]
	v_add_f32_e32 v80, v88, v80
	v_add_f32_e32 v81, v88, v81
	v_add_f32_e32 v82, v88, v82
	v_add_f32_e32 v83, v88, v83
	v_add_f32_e32 v84, v89, v84
	v_add_f32_e32 v85, v89, v85
	v_add_f32_e32 v86, v89, v86
	v_add_f32_e32 v87, v89, v87
	v_add_f32_e32 v76, v76, v77
	v_add_f32_e32 v78, v78, v79
	v_add_f32_e32 v120, v120, v121
	v_add_f32_e32 v122, v122, v123
	v_mul_u32_u24_e32 v6, 0x1800, v1
	v_or_b32_e32 v6, v38, v6
	ds_write2st64_b32 v6, v80, v81 offset1:2
	ds_write2st64_b32 v6, v82, v83 offset0:4 offset1:6
	ds_write2st64_b32 v6, v76, v78 offset0:8 offset1:10
	ds_write2st64_b32 v6, v120, v122 offset0:12 offset1:14
	ds_write2st64_b32 v6, v84, v85 offset0:16 offset1:18
	ds_write2st64_b32 v6, v86, v87 offset0:20 offset1:22
	v_or_b32_e32 v10, 0xc000, v38
	v_lshl_or_b32 v11, v1, 9, v38
	v_add_u32_e32 v1, 4, v1
	v_mov_b32_e32 v12, v0
	s_mov_b64 s[4:5], 0
	s_movk_i32 s8, 0x1ff
	s_movk_i32 s9, 0x3ff
	s_waitcnt lgkmcnt(0)
	s_barrier
	s_branch .LBB2_21
